# DeltaNet chunk-local step 3 rewritten as straight-line code: wave-uniform decay terms by v_readlane, batched LDS reads, no per-element branches
# speedup vs baseline: 1.0134x; 1.0089x over previous
.LBB0_1475:
	s_or_b64 exec, exec, s[0:1]
	s_and_b32 s0, s10, 1
	s_cmp_lt_i32 s10, 4
	s_cselect_b64 vcc, -1, 0
	s_lshl_b32 s1, s10, 4
	v_and_b32_e32 v25, 31, v0
	s_and_b32 s1, s1, 32
	v_add_u32_e32 v1, 0x4800, v61
	v_lshrrev_b32_e32 v2, 5, v21
	v_or_b32_e32 v4, s1, v25
	v_cndmask_b32_e32 v1, v1, v61, vcc
	v_mul_u32_u24_e32 v4, 0x110, v4
	v_lshlrev_b32_e32 v5, 4, v2
	v_add3_u32 v1, v1, v4, v5
	v_lshl_or_b32 v4, s0, 5, v25
	v_mul_u32_u24_e32 v4, 0x110, v4
	v_add3_u32 v34, v61, v4, v5
	ds_read_b128 v[4:7], v1
	ds_read_b128 v[72:75], v1 offset:32
	ds_read_b128 v[8:11], v34
	ds_read_b128 v[76:79], v34 offset:32
	s_waitcnt lgkmcnt(1)
	v_mfma_f32_32x32x16_bf16 v[4:19], v[4:7], v[8:11], 0
	v_add_u32_e32 v31, 0x1f100, v61
	v_add_u32_e32 v32, 0x1b000, v61
	v_lshlrev_b32_e32 v35, 2, v25
	s_waitcnt lgkmcnt(0)
	v_mfma_f32_32x32x16_bf16 v[4:19], v[72:75], v[76:79], v[4:19]
	ds_read_b128 v[72:75], v1 offset:64
	ds_read_b128 v[76:79], v34 offset:64
	s_waitcnt lgkmcnt(0)
	v_mfma_f32_32x32x16_bf16 v[4:19], v[72:75], v[76:79], v[4:19]
	ds_read_b128 v[72:75], v1 offset:96
	ds_read_b128 v[76:79], v34 offset:96
	s_waitcnt lgkmcnt(0)
	v_mfma_f32_32x32x16_bf16 v[4:19], v[72:75], v[76:79], v[4:19]
	ds_read_b128 v[72:75], v1 offset:128
	ds_read_b128 v[76:79], v34 offset:128
	s_waitcnt lgkmcnt(0)
	v_mfma_f32_32x32x16_bf16 v[4:19], v[72:75], v[76:79], v[4:19]
	ds_read_b128 v[72:75], v1 offset:160
	ds_read_b128 v[76:79], v34 offset:160
	s_waitcnt lgkmcnt(0)
	v_mfma_f32_32x32x16_bf16 v[4:19], v[72:75], v[76:79], v[4:19]
	ds_read_b128 v[72:75], v1 offset:192
	ds_read_b128 v[76:79], v34 offset:192
	s_waitcnt lgkmcnt(0)
	v_mfma_f32_32x32x16_bf16 v[4:19], v[72:75], v[76:79], v[4:19]
	ds_read_b128 v[72:75], v1 offset:224
	ds_read_b128 v[76:79], v34 offset:224
	v_cndmask_b32_e32 v1, v31, v32, vcc
	v_lshl_or_b32 v34, v2, 2, s1
	v_lshl_add_u32 v1, s0, 7, v1
	v_mul_u32_u24_e32 v34, 0x104, v34
	v_add3_u32 v1, v1, v35, v34
	s_waitcnt lgkmcnt(0)
	v_mfma_f32_32x32x16_bf16 v[4:19], v[72:75], v[76:79], v[4:19]
	s_nop 11
	ds_write2_b32 v1, v4, v5 offset1:65
	ds_write2_b32 v1, v6, v7 offset0:130 offset1:195
	v_add_u32_e32 v4, 0x800, v1
	ds_write2_b32 v4, v8, v9 offset0:8 offset1:73
	ds_write2_b32 v4, v10, v11 offset0:138 offset1:203
	v_add_u32_e32 v4, 0x1000, v1
	v_add_u32_e32 v1, 0x1800, v1
	ds_write2_b32 v4, v12, v13 offset0:16 offset1:81
	ds_write2_b32 v4, v14, v15 offset0:146 offset1:211
	ds_write2_b32 v1, v16, v17 offset0:24 offset1:89
	ds_write2_b32 v1, v18, v19 offset0:154 offset1:219
	s_waitcnt lgkmcnt(0)
	s_barrier
	v_add_u32_e32 v4, v23, v28
	ds_read_b32 v5, v4
	ds_read_b32 v6, v4 offset:256
	ds_read_b32 v7, v4 offset:512
	ds_read_b32 v8, v4 offset:768
	s_mul_i32 s0, s10, 0x104
	s_sub_i32 s1, 7, s10
	v_lshlrev_b32_e32 v10, 2, v27
	s_mul_i32 s1, s1, 0x104
	v_add3_u32 v9, v32, v28, s0
	s_mul_i32 s11, s10, 0x110
	v_add3_u32 v10, v32, v10, s1
	v_add3_u32 v11, v61, v28, s11
	s_add_u32 s12, s46, s58
	s_addc_u32 s13, s47, s59
	v_lshlrev_b32_e32 v12, 1, v0
	s_add_u32 s12, s12, 0x402f8000
	s_addc_u32 s13, s13, 0
	v_add_u32_e32 v13, 0x1000, v12
	ds_read_b32 v72, v9 offset:0
	ds_read_b32 v80, v9 offset:16640
	ds_read_b32 v73, v9 offset:2080
	ds_read_b32 v81, v9 offset:18720
	ds_read_b32 v74, v9 offset:4160
	ds_read_b32 v82, v9 offset:20800
	ds_read_b32 v75, v9 offset:6240
	ds_read_b32 v83, v9 offset:22880
	ds_read_b32 v76, v9 offset:8320
	ds_read_b32 v84, v9 offset:24960
	s_waitcnt lgkmcnt(10)
	s_add_i32 s24, s10, 0
	v_readlane_b32 s40, v5, s24
	v_readlane_b32 s69, v7, s24
	s_add_i32 s24, s10, 8
	v_readlane_b32 s41, v5, s24
	v_readlane_b32 s70, v7, s24
	s_add_i32 s24, s10, 16
	v_readlane_b32 s42, v5, s24
	v_readlane_b32 s71, v7, s24
	s_add_i32 s24, s10, 24
	v_readlane_b32 s43, v5, s24
	v_readlane_b32 s76, v7, s24
	s_add_i32 s24, s10, 32
	v_readlane_b32 s48, v5, s24
	v_readlane_b32 s77, v7, s24
	s_add_i32 s24, s10, 40
	v_readlane_b32 s49, v5, s24
	v_readlane_b32 s78, v7, s24
	s_add_i32 s24, s10, 48
	v_readlane_b32 s62, v5, s24
	v_readlane_b32 s80, v7, s24
	s_add_i32 s24, s10, 56
	v_readlane_b32 s63, v5, s24
	v_readlane_b32 s82, v7, s24
	ds_read_b32 v77, v9 offset:10400
	ds_read_b32 v85, v9 offset:27040
	ds_read_b32 v78, v9 offset:12480
	ds_read_b32 v86, v9 offset:29120
	ds_read_b32 v79, v9 offset:14560
	ds_read_b32 v87, v9 offset:31200
	v_sub_f32_e32 v14, s40, v5
	v_sub_f32_e32 v15, s41, v5
	v_sub_f32_e32 v16, s42, v5
	v_sub_f32_e32 v17, s43, v5
	v_sub_f32_e32 v18, s48, v5
	v_sub_f32_e32 v19, s49, v5
	v_sub_f32_e32 v34, s62, v5
	v_sub_f32_e32 v35, s63, v5
	v_mul_f32_e32 v14, 0x3fb8aa3b, v14
	v_mul_f32_e32 v15, 0x3fb8aa3b, v15
	v_mul_f32_e32 v16, 0x3fb8aa3b, v16
	v_mul_f32_e32 v17, 0x3fb8aa3b, v17
	v_mul_f32_e32 v18, 0x3fb8aa3b, v18
	v_mul_f32_e32 v19, 0x3fb8aa3b, v19
	v_mul_f32_e32 v34, 0x3fb8aa3b, v34
	v_mul_f32_e32 v35, 0x3fb8aa3b, v35
	v_exp_f32_e32 v14, v14
	v_exp_f32_e32 v15, v15
	v_exp_f32_e32 v16, v16
	v_exp_f32_e32 v17, v17
	v_exp_f32_e32 v18, v18
	v_exp_f32_e32 v19, v19
	v_exp_f32_e32 v34, v34
	v_exp_f32_e32 v35, v35
	s_nop 0
	s_add_i32 s24, s10, 0
	v_cmp_ge_u32_e32 vcc, s24, v21
	s_nop 1
	v_cndmask_b32_e32 v14, 0, v14, vcc
	s_add_i32 s24, s10, 8
	v_cmp_ge_u32_e32 vcc, s24, v21
	s_nop 1
	v_cndmask_b32_e32 v15, 0, v15, vcc
	s_add_i32 s24, s10, 16
	v_cmp_ge_u32_e32 vcc, s24, v21
	s_nop 1
	v_cndmask_b32_e32 v16, 0, v16, vcc
	s_add_i32 s24, s10, 24
	v_cmp_ge_u32_e32 vcc, s24, v21
	s_nop 1
	v_cndmask_b32_e32 v17, 0, v17, vcc
	s_add_i32 s24, s10, 32
	v_cmp_ge_u32_e32 vcc, s24, v21
	s_nop 1
	v_cndmask_b32_e32 v18, 0, v18, vcc
	s_add_i32 s24, s10, 40
	v_cmp_ge_u32_e32 vcc, s24, v21
	s_nop 1
	v_cndmask_b32_e32 v19, 0, v19, vcc
	s_add_i32 s24, s10, 48
	v_cmp_ge_u32_e32 vcc, s24, v21
	s_nop 1
	v_cndmask_b32_e32 v34, 0, v34, vcc
	s_add_i32 s24, s10, 56
	v_cmp_ge_u32_e32 vcc, s24, v21
	s_nop 1
	v_cndmask_b32_e32 v35, 0, v35, vcc
	s_waitcnt lgkmcnt(0)
	v_mul_f32_e32 v100, s69, v72
	v_mul_f32_e32 v80, 0x3db504f3, v80
	v_mul_f32_e32 v101, s70, v73
	v_mul_f32_e32 v81, 0x3db504f3, v81
	v_mul_f32_e32 v102, s71, v74
	v_mul_f32_e32 v82, 0x3db504f3, v82
	v_mul_f32_e32 v103, s76, v75
	v_mul_f32_e32 v83, 0x3db504f3, v83
	v_mul_f32_e32 v104, s77, v76
	v_mul_f32_e32 v84, 0x3db504f3, v84
	v_mul_f32_e32 v105, s78, v77
	v_mul_f32_e32 v85, 0x3db504f3, v85
	v_mul_f32_e32 v106, s80, v78
	v_mul_f32_e32 v86, 0x3db504f3, v86
	v_mul_f32_e32 v107, s82, v79
	v_mul_f32_e32 v87, 0x3db504f3, v87
	v_mul_f32_e32 v100, v14, v100
	v_mul_f32_e32 v80, v14, v80
	v_mul_f32_e32 v101, v15, v101
	v_mul_f32_e32 v81, v15, v81
	v_mul_f32_e32 v102, v16, v102
	v_mul_f32_e32 v82, v16, v82
	v_mul_f32_e32 v103, v17, v103
	v_mul_f32_e32 v83, v17, v83
	v_mul_f32_e32 v104, v18, v104
	v_mul_f32_e32 v84, v18, v84
	v_mul_f32_e32 v105, v19, v105
	v_mul_f32_e32 v85, v19, v85
	v_mul_f32_e32 v106, v34, v106
	v_mul_f32_e32 v86, v34, v86
	v_mul_f32_e32 v107, v35, v107
	v_mul_f32_e32 v87, v35, v87
	s_add_i32 s24, s10, 0
	v_cmp_gt_u32_e32 vcc, s24, v21
	v_cvt_pk_bf16_f32 v80, v80, v80
	s_nop 0
	v_cndmask_b32_e32 v100, 0, v100, vcc
	s_add_i32 s24, s10, 8
	v_cmp_gt_u32_e32 vcc, s24, v21
	v_cvt_pk_bf16_f32 v81, v81, v81
	s_nop 0
	v_cndmask_b32_e32 v101, 0, v101, vcc
	s_add_i32 s24, s10, 16
	v_cmp_gt_u32_e32 vcc, s24, v21
	v_cvt_pk_bf16_f32 v82, v82, v82
	s_nop 0
	v_cndmask_b32_e32 v102, 0, v102, vcc
	s_add_i32 s24, s10, 24
	v_cmp_gt_u32_e32 vcc, s24, v21
	v_cvt_pk_bf16_f32 v83, v83, v83
	s_nop 0
	v_cndmask_b32_e32 v103, 0, v103, vcc
	s_add_i32 s24, s10, 32
	v_cmp_gt_u32_e32 vcc, s24, v21
	v_cvt_pk_bf16_f32 v84, v84, v84
	s_nop 0
	v_cndmask_b32_e32 v104, 0, v104, vcc
	s_add_i32 s24, s10, 40
	v_cmp_gt_u32_e32 vcc, s24, v21
	v_cvt_pk_bf16_f32 v85, v85, v85
	s_nop 0
	v_cndmask_b32_e32 v105, 0, v105, vcc
	s_add_i32 s24, s10, 48
	v_cmp_gt_u32_e32 vcc, s24, v21
	v_cvt_pk_bf16_f32 v86, v86, v86
	s_nop 0
	v_cndmask_b32_e32 v106, 0, v106, vcc
	s_add_i32 s24, s10, 56
	v_cmp_gt_u32_e32 vcc, s24, v21
	v_cvt_pk_bf16_f32 v87, v87, v87
	s_nop 0
	v_cndmask_b32_e32 v107, 0, v107, vcc
	ds_write_b32 v11, v100 offset:0
	ds_write_b32 v11, v101 offset:2176
	ds_write_b32 v11, v102 offset:4352
	ds_write_b32 v11, v103 offset:6528
	ds_write_b32 v11, v104 offset:8704
	ds_write_b32 v11, v105 offset:10880
	ds_write_b32 v11, v106 offset:13056
	ds_write_b32 v11, v107 offset:15232
	global_store_short v12, v80, s[12:13] offset:0
	global_store_short v12, v81, s[12:13] offset:1024
	global_store_short v12, v82, s[12:13] offset:2048
	global_store_short v12, v83, s[12:13] offset:3072
	global_store_short v13, v84, s[12:13] offset:0
	global_store_short v13, v85, s[12:13] offset:1024
	global_store_short v13, v86, s[12:13] offset:2048
	global_store_short v13, v87, s[12:13] offset:3072
	s_add_u32 s12, s12, 0x2000
	s_addc_u32 s13, s13, 0
	ds_read_b32 v72, v10 offset:14560
	ds_read_b32 v80, v10 offset:31200
	ds_read_b32 v73, v10 offset:12480
	ds_read_b32 v81, v10 offset:29120
	ds_read_b32 v74, v10 offset:10400
	ds_read_b32 v82, v10 offset:27040
	ds_read_b32 v75, v10 offset:8320
	ds_read_b32 v83, v10 offset:24960
	ds_read_b32 v76, v10 offset:6240
	ds_read_b32 v84, v10 offset:22880
	s_add_i32 s24, s10, 0
	v_readlane_b32 s40, v6, s24
	v_readlane_b32 s69, v8, s24
	s_add_i32 s24, s10, 8
	v_readlane_b32 s41, v6, s24
	v_readlane_b32 s70, v8, s24
	s_add_i32 s24, s10, 16
	v_readlane_b32 s42, v6, s24
	v_readlane_b32 s71, v8, s24
	s_add_i32 s24, s10, 24
	v_readlane_b32 s43, v6, s24
	v_readlane_b32 s76, v8, s24
	s_add_i32 s24, s10, 32
	v_readlane_b32 s48, v6, s24
	v_readlane_b32 s77, v8, s24
	s_add_i32 s24, s10, 40
	v_readlane_b32 s49, v6, s24
	v_readlane_b32 s78, v8, s24
	s_add_i32 s24, s10, 48
	v_readlane_b32 s62, v6, s24
	v_readlane_b32 s80, v8, s24
	s_add_i32 s24, s10, 56
	v_readlane_b32 s63, v6, s24
	v_readlane_b32 s82, v8, s24
	ds_read_b32 v77, v10 offset:4160
	ds_read_b32 v85, v10 offset:20800
	ds_read_b32 v78, v10 offset:2080
	ds_read_b32 v86, v10 offset:18720
	ds_read_b32 v79, v10 offset:0
	ds_read_b32 v87, v10 offset:16640
	v_sub_f32_e32 v14, s40, v6
	v_sub_f32_e32 v15, s41, v6
	v_sub_f32_e32 v16, s42, v6
	v_sub_f32_e32 v17, s43, v6
	v_sub_f32_e32 v18, s48, v6
	v_sub_f32_e32 v19, s49, v6
	v_sub_f32_e32 v34, s62, v6
	v_sub_f32_e32 v35, s63, v6
	v_mul_f32_e32 v14, 0x3fb8aa3b, v14
	v_mul_f32_e32 v15, 0x3fb8aa3b, v15
	v_mul_f32_e32 v16, 0x3fb8aa3b, v16
	v_mul_f32_e32 v17, 0x3fb8aa3b, v17
	v_mul_f32_e32 v18, 0x3fb8aa3b, v18
	v_mul_f32_e32 v19, 0x3fb8aa3b, v19
	v_mul_f32_e32 v34, 0x3fb8aa3b, v34
	v_mul_f32_e32 v35, 0x3fb8aa3b, v35
	v_exp_f32_e32 v14, v14
	v_exp_f32_e32 v15, v15
	v_exp_f32_e32 v16, v16
	v_exp_f32_e32 v17, v17
	v_exp_f32_e32 v18, v18
	v_exp_f32_e32 v19, v19
	v_exp_f32_e32 v34, v34
	v_exp_f32_e32 v35, v35
	s_nop 0
	s_add_i32 s24, s10, 0
	v_cmp_ge_u32_e32 vcc, s24, v21
	s_nop 1
	v_cndmask_b32_e32 v14, 0, v14, vcc
	s_add_i32 s24, s10, 8
	v_cmp_ge_u32_e32 vcc, s24, v21
	s_nop 1
	v_cndmask_b32_e32 v15, 0, v15, vcc
	s_add_i32 s24, s10, 16
	v_cmp_ge_u32_e32 vcc, s24, v21
	s_nop 1
	v_cndmask_b32_e32 v16, 0, v16, vcc
	s_add_i32 s24, s10, 24
	v_cmp_ge_u32_e32 vcc, s24, v21
	s_nop 1
	v_cndmask_b32_e32 v17, 0, v17, vcc
	s_add_i32 s24, s10, 32
	v_cmp_ge_u32_e32 vcc, s24, v21
	s_nop 1
	v_cndmask_b32_e32 v18, 0, v18, vcc
	s_add_i32 s24, s10, 40
	v_cmp_ge_u32_e32 vcc, s24, v21
	s_nop 1
	v_cndmask_b32_e32 v19, 0, v19, vcc
	s_add_i32 s24, s10, 48
	v_cmp_ge_u32_e32 vcc, s24, v21
	s_nop 1
	v_cndmask_b32_e32 v34, 0, v34, vcc
	s_add_i32 s24, s10, 56
	v_cmp_ge_u32_e32 vcc, s24, v21
	s_nop 1
	v_cndmask_b32_e32 v35, 0, v35, vcc
	s_waitcnt lgkmcnt(0)
	v_mul_f32_e32 v100, s69, v72
	v_mul_f32_e32 v80, 0x3db504f3, v80
	v_mul_f32_e32 v101, s70, v73
	v_mul_f32_e32 v81, 0x3db504f3, v81
	v_mul_f32_e32 v102, s71, v74
	v_mul_f32_e32 v82, 0x3db504f3, v82
	v_mul_f32_e32 v103, s76, v75
	v_mul_f32_e32 v83, 0x3db504f3, v83
	v_mul_f32_e32 v104, s77, v76
	v_mul_f32_e32 v84, 0x3db504f3, v84
	v_mul_f32_e32 v105, s78, v77
	v_mul_f32_e32 v85, 0x3db504f3, v85
	v_mul_f32_e32 v106, s80, v78
	v_mul_f32_e32 v86, 0x3db504f3, v86
	v_mul_f32_e32 v107, s82, v79
	v_mul_f32_e32 v87, 0x3db504f3, v87
	v_mul_f32_e32 v100, v14, v100
	v_mul_f32_e32 v80, v14, v80
	v_mul_f32_e32 v101, v15, v101
	v_mul_f32_e32 v81, v15, v81
	v_mul_f32_e32 v102, v16, v102
	v_mul_f32_e32 v82, v16, v82
	v_mul_f32_e32 v103, v17, v103
	v_mul_f32_e32 v83, v17, v83
	v_mul_f32_e32 v104, v18, v104
	v_mul_f32_e32 v84, v18, v84
	v_mul_f32_e32 v105, v19, v105
	v_mul_f32_e32 v85, v19, v85
	v_mul_f32_e32 v106, v34, v106
	v_mul_f32_e32 v86, v34, v86
	v_mul_f32_e32 v107, v35, v107
	v_mul_f32_e32 v87, v35, v87
	s_add_i32 s24, s10, 0
	v_cmp_gt_u32_e32 vcc, s24, v21
	v_cvt_pk_bf16_f32 v80, v80, v80
	s_nop 0
	v_cndmask_b32_e32 v100, 0, v100, vcc
	s_add_i32 s24, s10, 8
	v_cmp_gt_u32_e32 vcc, s24, v21
	v_cvt_pk_bf16_f32 v81, v81, v81
	s_nop 0
	v_cndmask_b32_e32 v101, 0, v101, vcc
	s_add_i32 s24, s10, 16
	v_cmp_gt_u32_e32 vcc, s24, v21
	v_cvt_pk_bf16_f32 v82, v82, v82
	s_nop 0
	v_cndmask_b32_e32 v102, 0, v102, vcc
	s_add_i32 s24, s10, 24
	v_cmp_gt_u32_e32 vcc, s24, v21
	v_cvt_pk_bf16_f32 v83, v83, v83
	s_nop 0
	v_cndmask_b32_e32 v103, 0, v103, vcc
	s_add_i32 s24, s10, 32
	v_cmp_gt_u32_e32 vcc, s24, v21
	v_cvt_pk_bf16_f32 v84, v84, v84
	s_nop 0
	v_cndmask_b32_e32 v104, 0, v104, vcc
	s_add_i32 s24, s10, 40
	v_cmp_gt_u32_e32 vcc, s24, v21
	v_cvt_pk_bf16_f32 v85, v85, v85
	s_nop 0
	v_cndmask_b32_e32 v105, 0, v105, vcc
	s_add_i32 s24, s10, 48
	v_cmp_gt_u32_e32 vcc, s24, v21
	v_cvt_pk_bf16_f32 v86, v86, v86
	s_nop 0
	v_cndmask_b32_e32 v106, 0, v106, vcc
	s_add_i32 s24, s10, 56
	v_cmp_gt_u32_e32 vcc, s24, v21
	v_cvt_pk_bf16_f32 v87, v87, v87
	s_nop 0
	v_cndmask_b32_e32 v107, 0, v107, vcc
	ds_write_b32 v11, v100 offset:18432
	ds_write_b32 v11, v101 offset:20608
	ds_write_b32 v11, v102 offset:22784
	ds_write_b32 v11, v103 offset:24960
	ds_write_b32 v11, v104 offset:27136
	ds_write_b32 v11, v105 offset:29312
	ds_write_b32 v11, v106 offset:31488
	ds_write_b32 v11, v107 offset:33664
	global_store_short v12, v80, s[12:13] offset:0
	global_store_short v12, v81, s[12:13] offset:1024
	global_store_short v12, v82, s[12:13] offset:2048
	global_store_short v12, v83, s[12:13] offset:3072
	global_store_short v13, v84, s[12:13] offset:0
	global_store_short v13, v85, s[12:13] offset:1024
	global_store_short v13, v86, s[12:13] offset:2048
	global_store_short v13, v87, s[12:13] offset:3072
	s_and_saveexec_b64 s[0:1], s[38:39]
	s_cbranch_execz .LBB0_1574
	ds_read_b32 v5, v30
	v_add_u32_e32 v1, v23, v29
	ds_read_b32 v1, v1
	s_movk_i32 s11, 0xc0
	v_mul_lo_u32 v4, v26, s11
	s_waitcnt lgkmcnt(1)
	v_mul_f32_e32 v6, 0x3fb8aa3b, v5
	v_exp_f32_e32 v8, v6
	s_add_u32 s12, s46, s9
	v_or_b32_e32 v6, v4, v21
	s_addc_u32 s13, s47, s8
	v_ashrrev_i32_e32 v7, 31, v6
	v_mul_f32_e32 v10, 0x3db504f3, v8
	v_lshl_add_u64 v[8:9], v[6:7], 2, s[12:13]
	s_mov_b32 s11, 0x424f8000
	v_add_co_u32_e32 v8, vcc, s11, v8
	s_waitcnt lgkmcnt(0)
	v_sub_f32_e32 v5, v1, v5
	v_addc_co_u32_e32 v9, vcc, 0, v9, vcc
	v_mul_f32_e32 v5, 0x3fb8aa3b, v5
	global_store_dword v[8:9], v10, off
	v_exp_f32_e32 v8, v5
	v_ashrrev_i32_e32 v5, 31, v4
	v_mov_b32_e32 v7, v5
	v_lshl_add_u64 v[6:7], v[6:7], 2, s[12:13]
	v_add_co_u32_e32 v6, vcc, 0x424f8000, v6
	s_nop 1
	v_addc_co_u32_e32 v7, vcc, 0, v7, vcc
	v_cmp_eq_u32_e32 vcc, 0, v21
	global_store_dword v[6:7], v8, off offset:256
	s_and_b64 exec, exec, vcc
	s_cbranch_execz .LBB0_1574
	s_add_u32 s12, s46, s9
	v_mul_f32_e32 v1, 0x3fb8aa3b, v1
	s_addc_u32 s13, s47, s8
	v_exp_f32_e32 v1, v1
	v_lshl_add_u64 v[4:5], v[4:5], 2, s[12:13]
	v_add_co_u32_e32 v4, vcc, 0x424f8000, v4
	s_nop 1
	v_addc_co_u32_e32 v5, vcc, 0, v5, vcc
	global_store_dword v[4:5], v1, off offset:512
